# Hyena-phase conversion hook loads without the nt hint (on top of v6)
# speedup vs baseline: 1.0077x; 1.0024x over previous
.LBB0_746:
	s_lshl_b64 s[4:5], s[4:5], 13
	s_add_u32 s4, s8, s4
	s_addc_u32 s5, s9, s5
	s_lshl_b32 s6, s12, s7
	s_and_b32 s6, s6, 0x700
	s_lshl_b32 s6, s6, 2
	s_add_u32 s4, s4, s6
	s_addc_u32 s5, s5, 0
	s_cmp_lt_i32 s59, 0
	v_lshlrev_b32_e32 v0, 2, v192
	v_and_b32_e32 v180, 0xfc, v0
	s_cselect_b64 s[6:7], -1, 0
	v_cndmask_b32_e64 v0, v180, 0, s[6:7]
	s_and_b64 s[6:7], s[6:7], exec
	v_ashrrev_i32_e32 v6, 3, v192
	s_cselect_b32 s6, 0, 0x800
	v_and_b32_e32 v181, -8, v6
	v_lshlrev_b32_e32 v0, 2, v0
	v_mov_b32_e32 v1, 0
	v_lshl_add_u64 v[0:1], s[4:5], 0, v[0:1]
	v_mad_i64_i32 v[2:3], s[4:5], s6, v181, 0
	v_or_b32_e32 v182, 1, v181
	v_lshl_add_u64 v[2:3], v[2:3], 2, v[0:1]
	v_mad_i64_i32 v[4:5], s[4:5], s6, v182, 0
	v_or_b32_e32 v183, 2, v181
	v_lshl_add_u64 v[4:5], v[4:5], 2, v[0:1]
	global_load_dwordx4 v[48:51], v[2:3], off
	global_load_dwordx4 v[52:55], v[4:5], off
	v_mad_i64_i32 v[2:3], s[4:5], s6, v183, 0
	v_or_b32_e32 v184, 3, v181
	v_lshl_add_u64 v[2:3], v[2:3], 2, v[0:1]
	v_mad_i64_i32 v[4:5], s[4:5], s6, v184, 0
	v_or_b32_e32 v185, 4, v181
	v_lshl_add_u64 v[4:5], v[4:5], 2, v[0:1]
	global_load_dwordx4 v[64:67], v[2:3], off
	global_load_dwordx4 v[68:71], v[4:5], off
	v_mad_i64_i32 v[2:3], s[4:5], s6, v185, 0
	s_waitcnt vmcnt(0)
	v_or_b32_e32 v186, 5, v181
	v_lshl_add_u64 v[2:3], v[2:3], 2, v[0:1]
	v_mad_i64_i32 v[4:5], s[4:5], s6, v186, 0
	v_or_b32_e32 v187, 6, v181
	v_lshl_add_u64 v[4:5], v[4:5], 2, v[0:1]
	global_load_dwordx4 v[40:43], v[2:3], off
	global_load_dwordx4 v[44:47], v[4:5], off
	v_mad_i64_i32 v[2:3], s[4:5], s6, v187, 0
	v_or_b32_e32 v188, 7, v6
	v_lshl_add_u64 v[2:3], v[2:3], 2, v[0:1]
	v_mad_i64_i32 v[4:5], s[4:5], s6, v188, 0
	v_lshl_add_u64 v[0:1], v[4:5], 2, v[0:1]
	global_load_dwordx4 v[56:59], v[2:3], off
	global_load_dwordx4 v[60:63], v[0:1], off
	s_min_i32 s4, s59, 1
	s_mul_i32 s4, s4, s3
	s_add_i32 s5, s4, s2
	s_mul_hi_i32 s4, s5, 0x2aaaaaab
	s_lshr_b32 s6, s4, 31
	s_ashr_i32 s4, s4, 7
	s_add_i32 s6, s4, s6
	s_add_i32 s4, s6, 10
	s_mulk_i32 s6, 0x300
	s_sub_i32 s12, s5, s6
	v_readlane_b32 s88, v255, 6
	v_readlane_b32 s90, v255, 3
	s_cmpk_gt_i32 s12, 0x1ff
	s_mov_b32 s7, 0
	v_readlane_b32 s89, v255, 7
	v_readlane_b32 s85, v255, 5
	v_readlane_b32 s91, v255, 4
	s_cbranch_scc0 .LBB0_748
	s_load_dwordx2 s[8:9], s[14:15], 0x110
	s_ashr_i32 s5, s4, 31
	s_lshl_b64 s[10:11], s[4:5], 24
	s_waitcnt lgkmcnt(0)
	s_add_u32 s8, s8, s10
	s_addc_u32 s9, s9, s11
	s_lshl_b32 s5, s12, 3
	s_and_b32 s5, s5, 0x7fffffc0
	s_add_i32 s6, s5, 0xfffff000
	s_load_dwordx2 s[16:17], s[0:1], 0x138
	s_mov_b32 s0, 8
	s_cbranch_execz .LBB0_749
	s_branch .LBB0_750

.LBB0_750:
	s_lshl_b64 s[4:5], s[6:7], 13
	s_add_u32 s1, s8, s4
	s_addc_u32 s4, s9, s5
	s_lshl_b32 s0, s12, s0
	s_and_b32 s0, s0, 0x700
	s_lshl_b32 s0, s0, 2
	s_add_u32 s0, s1, s0
	s_addc_u32 s1, s4, 0
	s_cmp_lt_i32 s59, 1
	s_cselect_b64 s[4:5], -1, 0
	v_cndmask_b32_e64 v0, v180, 0, s[4:5]
	s_and_b64 s[4:5], s[4:5], exec
	s_cselect_b32 s4, 0, 0x800
	v_lshlrev_b32_e32 v86, 2, v0
	v_mov_b32_e32 v87, 0
	v_lshl_add_u64 v[0:1], s[0:1], 0, v[86:87]
	v_mad_i64_i32 v[2:3], s[0:1], s4, v181, 0
	v_lshl_add_u64 v[2:3], v[2:3], 2, v[0:1]
	v_mad_i64_i32 v[4:5], s[0:1], s4, v182, 0
	v_lshl_add_u64 v[4:5], v[4:5], 2, v[0:1]
	global_load_dwordx4 v[20:23], v[2:3], off
	global_load_dwordx4 v[16:19], v[4:5], off
	v_mad_i64_i32 v[2:3], s[0:1], s4, v183, 0
	v_lshl_add_u64 v[2:3], v[2:3], 2, v[0:1]
	v_mad_i64_i32 v[4:5], s[0:1], s4, v184, 0
	v_lshl_add_u64 v[4:5], v[4:5], 2, v[0:1]
	global_load_dwordx4 v[36:39], v[2:3], off
	global_load_dwordx4 v[32:35], v[4:5], off
	v_mad_i64_i32 v[2:3], s[0:1], s4, v185, 0
	v_lshl_add_u64 v[2:3], v[2:3], 2, v[0:1]
	v_mad_i64_i32 v[4:5], s[0:1], s4, v186, 0
	v_lshl_add_u64 v[4:5], v[4:5], 2, v[0:1]
	global_load_dwordx4 v[12:15], v[2:3], off
	global_load_dwordx4 v[8:11], v[4:5], off
	v_mad_i64_i32 v[2:3], s[0:1], s4, v187, 0
	v_lshl_add_u64 v[2:3], v[2:3], 2, v[0:1]
	v_mad_i64_i32 v[4:5], s[0:1], s4, v188, 0
	v_lshl_add_u64 v[0:1], v[4:5], 2, v[0:1]
	global_load_dwordx4 v[28:31], v[2:3], off
	global_load_dwordx4 v[24:27], v[0:1], off
	s_mov_b32 s62, 2
	s_mov_b32 s18, 0
	s_cmpk_gt_i32 s2, 0x1ff
	v_bfe_u32 v189, v192, 2, 7
	v_ashrrev_i32_e32 v254, 5, v192
	v_lshlrev_b32_e32 v1, 4, v192
	v_and_b32_e32 v193, 3, v192
	v_and_b32_e32 v190, -4, v192
	v_ashrrev_i32_e32 v191, 9, v192
	s_cbranch_scc1 .LBB0_933
	s_waitcnt lgkmcnt(0)
	s_add_u32 s20, s16, 0x45300000
	s_addc_u32 s21, s17, 0
	s_add_i32 s0, 0, 0x1d000
	s_add_u32 s63, s16, 0x4e00000
	v_and_b32_e32 v0, 0xffffffe, v254
	s_movk_i32 s1, 0x410
	s_addc_u32 s64, s17, 0
	v_mul_lo_u32 v197, v0, s1
	v_or_b32_e32 v0, 1, v254
	s_add_u32 s65, s16, 0x75c00000
	v_mul_lo_u32 v198, v0, s1
	s_addc_u32 s66, s17, 0
	s_add_i32 s1, 0, 0x21100
	s_movk_i32 s4, 0x1040
	v_mov_b32_e32 v0, s1
	v_mad_u32_u24 v199, v193, s4, v0
	v_add_u32_e32 v0, 0x200, v192
	s_mov_b32 s26, -1.0
	v_and_b32_e32 v1, 0x3f0, v1
	v_and_b32_e32 v200, -4, v0
	v_ashrrev_i32_e32 v201, 9, v0
	v_mov_b32_e32 v0, s0
	s_add_u32 s22, s16, 0x5a700000
	s_brev_b32 s24, 61
	s_mov_b32 s27, 1.0
	s_mov_b32 s34, 0x3f6c835e
	s_mov_b32 s36, 0xbf3504f3
	v_add_u32_e32 v196, s0, v1
	v_lshlrev_b32_e32 v88, 4, v193
	v_mov_b32_e32 v89, v87
	v_add_u32_e32 v202, s1, v1
	v_mad_u32_u24 v203, v193, s4, v0
	s_addc_u32 s23, s17, 0
	s_lshl_b32 s67, s2, 1
	s_lshl_b32 s68, s3, 1
	s_mov_b32 s25, 0xba000000
	s_mov_b32 s69, 0x7f800000
	v_mov_b32_e32 v204, 0xbf1f24be
	v_mov_b32_e32 v205, 0x3e642e9d
	s_movk_i32 s70, 0xc00
	s_add_i32 s71, 0, 0x25200
	s_add_i32 s72, 0, 0x11000
	s_brev_b32 s73, 1
	s_mov_b32 s28, s27
	s_mov_b32 s29, s26
	s_mov_b32 s30, 0xbec3ef15
	s_mov_b32 s35, 0x3ec3ef15
	s_mov_b32 s37, 0x3f3504f3
	s_mov_b32 s38, 0xbf6c835e
	s_movk_i32 s74, 0xf0
	s_mov_b32 s75, 0xc3e00000
	v_mov_b32_e32 v206, 0x400
	v_mov_b32_e32 v207, 0x800
	v_mov_b32_e32 v208, 0x7fc00000
	v_mov_b32_e32 v209, 0x1800000
	v_mov_b32_e32 v210, 9
	v_mov_b32_e32 v211, 0x42800000
	v_mov_b32_e32 v212, 0x42000000
	v_mov_b32_e32 v213, 0x43e00000
	s_mov_b32 s80, s2
	s_branch .LBB0_753

.LBB0_809:
	s_lshl_b64 s[8:9], s[8:9], 13
	s_add_u32 s0, s6, s8
	s_addc_u32 s7, s7, s9
	s_lshl_b32 s1, s19, s1
	s_and_b32 s1, s1, 0x700
	s_lshl_b32 s1, s1, 2
	s_add_u32 s6, s0, s1
	s_addc_u32 s7, s7, 0
	s_cmp_gt_i32 s62, s59
	s_cselect_b64 s[0:1], -1, 0
	v_cndmask_b32_e64 v0, v180, 0, s[0:1]
	s_and_b64 s[8:9], s[0:1], exec
	s_cselect_b32 s8, 0, 0x800
	v_lshlrev_b32_e32 v86, 2, v0
	v_lshl_add_u64 v[40:41], s[6:7], 0, v[86:87]
	v_mad_i64_i32 v[0:1], s[6:7], s8, v181, 0
	v_mad_i64_i32 v[2:3], s[6:7], s8, v182, 0
	v_lshl_add_u64 v[0:1], v[0:1], 2, v[40:41]
	v_lshl_add_u64 v[2:3], v[2:3], 2, v[40:41]
	global_load_dwordx4 v[48:51], v[0:1], off
	global_load_dwordx4 v[52:55], v[2:3], off
	v_mad_i64_i32 v[0:1], s[6:7], s8, v183, 0
	v_mad_i64_i32 v[2:3], s[6:7], s8, v184, 0
	v_lshl_add_u64 v[0:1], v[0:1], 2, v[40:41]
	v_lshl_add_u64 v[2:3], v[2:3], 2, v[40:41]
	global_load_dwordx4 v[56:59], v[0:1], off
	global_load_dwordx4 v[60:63], v[2:3], off
	v_mad_i64_i32 v[0:1], s[6:7], s8, v185, 0
	v_mad_i64_i32 v[2:3], s[6:7], s8, v186, 0
	v_mad_i64_i32 v[42:43], s[6:7], s8, v187, 0
	v_mad_i64_i32 v[44:45], s[6:7], s8, v188, 0
	v_lshl_add_u64 v[0:1], v[0:1], 2, v[40:41]
	v_lshl_add_u64 v[4:5], v[2:3], 2, v[40:41]
	v_lshl_add_u64 v[42:43], v[42:43], 2, v[40:41]
	v_lshl_add_u64 v[44:45], v[44:45], 2, v[40:41]
	global_load_dwordx4 v[0:3], v[0:1], off
	s_nop 0
	global_load_dwordx4 v[4:7], v[4:5], off
	s_nop 0
	global_load_dwordx4 v[40:43], v[42:43], off
	s_nop 0
	global_load_dwordx4 v[44:47], v[44:45], off
	s_add_i32 s19, s62, -3
	s_cmp_gt_i32 s62, 2
	s_cselect_b32 s6, s19, 0
	s_min_i32 s6, s6, s59
	s_mul_i32 s6, s6, s3
	s_add_i32 s7, s6, s2
	s_mul_hi_i32 s6, s7, 0x2aaaaaab
	s_lshr_b32 s8, s6, 31
	s_ashr_i32 s6, s6, 7
	s_add_i32 s8, s6, s8
	s_add_i32 s6, s8, 10
	s_mulk_i32 s8, 0x300
	s_sub_i32 s31, s7, s8
	s_ashr_i32 s7, s6, 31
	s_cmpk_gt_i32 s31, 0x1ff
	s_mov_b64 s[12:13], -1
	s_cbranch_scc0 .LBB0_811
	s_lshl_b32 s8, s31, 3
	s_and_b32 s12, s8, 0x7fffffc0
	s_lshl_b32 s8, s31, 19
	s_and_b32 s13, s8, 0x380000
	s_lshl_b64 s[8:9], s[6:7], 22
	s_add_u32 s8, s16, s8
	s_addc_u32 s9, s17, s9
	s_add_u32 s8, s8, s13
	s_addc_u32 s9, s9, 0
	s_add_u32 s8, s8, s12
	s_addc_u32 s9, s9, 0
	s_add_u32 s8, s8, 0x24dff000
	s_addc_u32 s9, s9, 0
	s_mov_b64 s[12:13], 0

.LBB0_817:
	s_lshl_b64 s[50:51], s[50:51], 13
	s_add_u32 s6, s12, s50
	s_addc_u32 s12, s13, s51
	s_lshl_b32 s7, s31, s7
	s_and_b32 s7, s7, 0x700
	s_lshl_b32 s7, s7, 2
	s_add_u32 s6, s6, s7
	s_addc_u32 s7, s12, 0
	s_cmp_ge_i32 s62, s59
	s_cselect_b64 s[54:55], -1, 0
	v_cndmask_b32_e64 v8, v180, 0, s[54:55]
	s_and_b64 s[12:13], s[54:55], exec
	s_cselect_b32 s12, 0, 0x800
	v_lshlrev_b32_e32 v86, 2, v8
	v_lshl_add_u64 v[8:9], s[6:7], 0, v[86:87]
	v_mad_i64_i32 v[10:11], s[6:7], s12, v181, 0
	v_mad_i64_i32 v[12:13], s[6:7], s12, v182, 0
	v_lshl_add_u64 v[10:11], v[10:11], 2, v[8:9]
	v_lshl_add_u64 v[12:13], v[12:13], 2, v[8:9]
	global_load_dwordx4 v[32:35], v[10:11], off
	global_load_dwordx4 v[36:39], v[12:13], off
	v_mad_i64_i32 v[10:11], s[6:7], s12, v183, 0
	v_mad_i64_i32 v[12:13], s[6:7], s12, v184, 0
	v_lshl_add_u64 v[10:11], v[10:11], 2, v[8:9]
	v_lshl_add_u64 v[12:13], v[12:13], 2, v[8:9]
	global_load_dwordx4 v[24:27], v[10:11], off
	global_load_dwordx4 v[28:31], v[12:13], off
	v_mad_i64_i32 v[10:11], s[6:7], s12, v185, 0
	v_mad_i64_i32 v[12:13], s[6:7], s12, v186, 0
	v_lshl_add_u64 v[10:11], v[10:11], 2, v[8:9]
	v_lshl_add_u64 v[12:13], v[12:13], 2, v[8:9]
	global_load_dwordx4 v[16:19], v[10:11], off
	global_load_dwordx4 v[20:23], v[12:13], off
	v_mad_i64_i32 v[10:11], s[6:7], s12, v187, 0
	v_mad_i64_i32 v[12:13], s[6:7], s12, v188, 0
	v_lshl_add_u64 v[10:11], v[10:11], 2, v[8:9]
	v_lshl_add_u64 v[12:13], v[12:13], 2, v[8:9]
	global_load_dwordx4 v[8:11], v[10:11], off
	s_nop 0
	global_load_dwordx4 v[12:15], v[12:13], off
	s_cmp_gt_i32 s62, 1
	s_cselect_b32 s6, s56, 0
	s_min_i32 s6, s6, s59
	s_mul_i32 s6, s6, s3
	s_add_i32 s7, s6, s2
	s_mul_hi_i32 s6, s7, 0x2aaaaaab
	s_lshr_b32 s12, s6, 31
	s_ashr_i32 s6, s6, 7
	s_add_i32 s12, s6, s12
	s_add_i32 s6, s12, 10
	s_mulk_i32 s12, 0x300
	s_sub_i32 s31, s7, s12
	s_ashr_i32 s7, s6, 31
	s_cmpk_gt_i32 s31, 0x1ff
	s_mov_b64 s[50:51], -1
	s_cbranch_scc0 .LBB0_819
	s_lshl_b32 s12, s31, 3
	s_and_b32 s33, s12, 0x7fffffc0
	s_lshl_b32 s12, s31, 19
	s_and_b32 s39, s12, 0x380000
	s_lshl_b64 s[12:13], s[6:7], 22
	s_add_u32 s12, s16, s12
	s_addc_u32 s13, s17, s13
	s_add_u32 s12, s12, s39
	s_addc_u32 s13, s13, 0
	s_add_u32 s12, s12, s33
	s_addc_u32 s13, s13, 0
	s_add_u32 s12, s12, 0x24dff000
	s_addc_u32 s13, s13, 0
	s_mov_b64 s[50:51], 0

.LBB0_825:
	s_lshl_b64 s[50:51], s[50:51], 13
	s_add_u32 s4, s12, s50
	s_addc_u32 s12, s13, s51
	s_lshl_b32 s5, s31, s5
	s_and_b32 s5, s5, 0x700
	s_lshl_b32 s5, s5, 2
	s_add_u32 s4, s4, s5
	s_addc_u32 s5, s12, 0
	s_add_i32 s56, s56, 4
	s_cmp_gt_i32 s56, s59
	s_cselect_b64 s[50:51], -1, 0
	v_cndmask_b32_e64 v0, v180, 0, s[50:51]
	s_and_b64 s[12:13], s[50:51], exec
	s_cselect_b32 s12, 0, 0x800
	v_lshlrev_b32_e32 v86, 2, v0
	v_lshl_add_u64 v[0:1], s[4:5], 0, v[86:87]
	v_mad_i64_i32 v[2:3], s[4:5], s12, v181, 0
	v_lshl_add_u64 v[2:3], v[2:3], 2, v[0:1]
	v_mad_i64_i32 v[4:5], s[4:5], s12, v182, 0
	v_lshl_add_u64 v[4:5], v[4:5], 2, v[0:1]
	global_load_dwordx4 v[56:59], v[2:3], off
	global_load_dwordx4 v[60:63], v[4:5], off
	v_mad_i64_i32 v[2:3], s[4:5], s12, v183, 0
	v_lshl_add_u64 v[2:3], v[2:3], 2, v[0:1]
	v_mad_i64_i32 v[4:5], s[4:5], s12, v184, 0
	v_lshl_add_u64 v[4:5], v[4:5], 2, v[0:1]
	global_load_dwordx4 v[64:67], v[2:3], off
	global_load_dwordx4 v[68:71], v[4:5], off
	v_mad_i64_i32 v[2:3], s[4:5], s12, v185, 0
	v_lshl_add_u64 v[2:3], v[2:3], 2, v[0:1]
	v_mad_i64_i32 v[4:5], s[4:5], s12, v186, 0
	v_lshl_add_u64 v[4:5], v[4:5], 2, v[0:1]
	global_load_dwordx4 v[40:43], v[2:3], off
	global_load_dwordx4 v[44:47], v[4:5], off
	v_mad_i64_i32 v[2:3], s[4:5], s12, v187, 0
	v_lshl_add_u64 v[2:3], v[2:3], 2, v[0:1]
	v_mad_i64_i32 v[4:5], s[4:5], s12, v188, 0
	v_lshl_add_u64 v[0:1], v[4:5], 2, v[0:1]
	global_load_dwordx4 v[48:51], v[2:3], off
	global_load_dwordx4 v[52:55], v[0:1], off
	s_cmp_gt_i32 s62, 0
	s_cselect_b32 s4, s19, 0
	s_min_i32 s4, s4, s59
	s_mul_i32 s4, s4, s3
	s_add_i32 s5, s4, s2
	s_mul_hi_i32 s4, s5, 0x2aaaaaab
	s_lshr_b32 s12, s4, 31
	s_ashr_i32 s4, s4, 7
	s_add_i32 s12, s4, s12
	s_add_i32 s4, s12, 10
	s_mulk_i32 s12, 0x300
	s_sub_i32 s31, s5, s12
	s_ashr_i32 s5, s4, 31
	s_cmpk_gt_i32 s31, 0x1ff
	s_mov_b64 s[52:53], -1
	s_cbranch_scc0 .LBB0_827
	s_lshl_b32 s12, s31, 3
	s_and_b32 s39, s12, 0x7fffffc0
	s_lshl_b32 s12, s31, 19
	s_and_b32 s52, s12, 0x380000
	s_lshl_b64 s[12:13], s[4:5], 22
	s_add_u32 s12, s16, s12
	s_addc_u32 s13, s17, s13
	s_add_u32 s12, s12, s52
	s_addc_u32 s13, s13, 0
	s_add_u32 s12, s12, s39
	s_addc_u32 s13, s13, 0
	s_add_u32 s12, s12, 0x24dff000
	s_addc_u32 s13, s13, 0
	s_mov_b64 s[52:53], 0

.LBB0_833:
	s_lshl_b64 s[52:53], s[52:53], 13
	s_add_u32 s8, s12, s52
	s_addc_u32 s12, s13, s53
	s_lshl_b32 s9, s31, s9
	s_and_b32 s9, s9, 0x700
	s_lshl_b32 s9, s9, 2
	s_add_u32 s8, s8, s9
	s_addc_u32 s9, s12, 0
	s_add_i32 s19, s19, 4
	s_cmp_gt_i32 s19, s59
	s_cselect_b64 s[52:53], -1, 0
	v_cndmask_b32_e64 v8, v180, 0, s[52:53]
	s_and_b64 s[12:13], s[52:53], exec
	s_cselect_b32 s12, 0, 0x800
	v_lshlrev_b32_e32 v86, 2, v8
	v_lshl_add_u64 v[16:17], s[8:9], 0, v[86:87]
	v_mad_i64_i32 v[8:9], s[8:9], s12, v181, 0
	v_mad_i64_i32 v[10:11], s[8:9], s12, v182, 0
	v_lshl_add_u64 v[8:9], v[8:9], 2, v[16:17]
	v_lshl_add_u64 v[10:11], v[10:11], 2, v[16:17]
	global_load_dwordx4 v[24:27], v[8:9], off
	global_load_dwordx4 v[28:31], v[10:11], off
	v_mad_i64_i32 v[8:9], s[8:9], s12, v183, 0
	v_mad_i64_i32 v[10:11], s[8:9], s12, v184, 0
	v_lshl_add_u64 v[8:9], v[8:9], 2, v[16:17]
	v_lshl_add_u64 v[10:11], v[10:11], 2, v[16:17]
	global_load_dwordx4 v[32:35], v[8:9], off
	global_load_dwordx4 v[36:39], v[10:11], off
	v_mad_i64_i32 v[8:9], s[8:9], s12, v185, 0
	v_mad_i64_i32 v[10:11], s[8:9], s12, v186, 0
	v_mad_i64_i32 v[18:19], s[8:9], s12, v187, 0
	v_mad_i64_i32 v[20:21], s[8:9], s12, v188, 0
	v_lshl_add_u64 v[8:9], v[8:9], 2, v[16:17]
	v_lshl_add_u64 v[12:13], v[10:11], 2, v[16:17]
	v_lshl_add_u64 v[18:19], v[18:19], 2, v[16:17]
	v_lshl_add_u64 v[20:21], v[20:21], 2, v[16:17]
	global_load_dwordx4 v[8:11], v[8:9], off
	s_nop 0
	global_load_dwordx4 v[12:15], v[12:13], off
	s_nop 0
	global_load_dwordx4 v[16:19], v[18:19], off
	s_nop 0
	global_load_dwordx4 v[20:23], v[20:21], off
	s_max_i32 s8, s62, 0
	s_min_i32 s8, s8, s59
	s_mul_i32 s8, s8, s3
	s_add_i32 s9, s8, s2
	s_mul_hi_i32 s8, s9, 0x2aaaaaab
	s_lshr_b32 s12, s8, 31
	s_ashr_i32 s8, s8, 7
	s_add_i32 s12, s8, s12
	s_add_i32 s8, s12, 10
	s_mulk_i32 s12, 0x300
	s_sub_i32 s19, s9, s12
	s_ashr_i32 s9, s8, 31
	s_cmpk_gt_i32 s19, 0x1ff
	s_mov_b64 s[56:57], -1
	s_cbranch_scc0 .LBB0_835
	s_lshl_b32 s12, s19, 3
	s_and_b32 s31, s12, 0x7fffffc0
	s_lshl_b32 s12, s19, 19
	s_and_b32 s39, s12, 0x380000
	s_lshl_b64 s[12:13], s[8:9], 22
	s_add_u32 s12, s16, s12
	s_addc_u32 s13, s17, s13
	s_add_u32 s12, s12, s39
	s_addc_u32 s13, s13, 0
	s_add_u32 s12, s12, s31
	s_addc_u32 s13, s13, 0
	s_add_u32 s12, s12, 0x24dff000
	s_addc_u32 s13, s13, 0
	s_mov_b64 s[56:57], 0

.LBB0_871:
	s_lshl_b64 s[12:13], s[12:13], 13
	s_add_u32 s0, s8, s12
	s_addc_u32 s9, s9, s13
	s_lshl_b32 s1, s19, s1
	s_and_b32 s1, s1, 0x700
	s_lshl_b32 s1, s1, 2
	s_add_u32 s8, s0, s1
	s_addc_u32 s9, s9, 0
	s_cmp_gt_i32 s78, s59
	s_cselect_b64 s[0:1], -1, 0
	v_cndmask_b32_e64 v40, v180, 0, s[0:1]
	s_and_b64 s[12:13], s[0:1], exec
	s_cselect_b32 s12, 0, 0x800
	v_lshlrev_b32_e32 v86, 2, v40
	v_lshl_add_u64 v[48:49], s[8:9], 0, v[86:87]
	v_mad_i64_i32 v[40:41], s[8:9], s12, v181, 0
	v_mad_i64_i32 v[42:43], s[8:9], s12, v182, 0
	v_lshl_add_u64 v[40:41], v[40:41], 2, v[48:49]
	v_lshl_add_u64 v[42:43], v[42:43], 2, v[48:49]
	global_load_dwordx4 v[56:59], v[40:41], off
	global_load_dwordx4 v[60:63], v[42:43], off
	v_mad_i64_i32 v[40:41], s[8:9], s12, v183, 0
	v_mad_i64_i32 v[42:43], s[8:9], s12, v184, 0
	v_lshl_add_u64 v[40:41], v[40:41], 2, v[48:49]
	v_lshl_add_u64 v[42:43], v[42:43], 2, v[48:49]
	global_load_dwordx4 v[64:67], v[40:41], off
	global_load_dwordx4 v[68:71], v[42:43], off
	v_mad_i64_i32 v[40:41], s[8:9], s12, v185, 0
	v_mad_i64_i32 v[42:43], s[8:9], s12, v186, 0
	v_mad_i64_i32 v[50:51], s[8:9], s12, v187, 0
	v_mad_i64_i32 v[52:53], s[8:9], s12, v188, 0
	v_lshl_add_u64 v[40:41], v[40:41], 2, v[48:49]
	v_lshl_add_u64 v[44:45], v[42:43], 2, v[48:49]
	v_lshl_add_u64 v[50:51], v[50:51], 2, v[48:49]
	v_lshl_add_u64 v[52:53], v[52:53], 2, v[48:49]
	global_load_dwordx4 v[40:43], v[40:41], off
	s_nop 0
	global_load_dwordx4 v[44:47], v[44:45], off
	s_nop 0
	global_load_dwordx4 v[48:51], v[50:51], off
	s_nop 0
	global_load_dwordx4 v[52:55], v[52:53], off
	s_cmp_gt_i32 s62, -2
	s_cselect_b32 s8, s76, 0
	s_min_i32 s8, s8, s59
	s_mul_i32 s8, s8, s3
	s_add_i32 s9, s8, s2
	s_mul_hi_i32 s8, s9, 0x2aaaaaab
	s_lshr_b32 s12, s8, 31
	s_ashr_i32 s8, s8, 7
	s_add_i32 s12, s8, s12
	s_add_i32 s8, s12, 10
	s_mulk_i32 s12, 0x300
	s_sub_i32 s19, s9, s12
	s_ashr_i32 s9, s8, 31
	s_cmpk_gt_i32 s19, 0x1ff
	s_mov_b64 s[56:57], -1
	s_cbranch_scc0 .LBB0_873
	s_lshl_b32 s12, s19, 3
	s_and_b32 s31, s12, 0x7fffffc0
	s_lshl_b32 s12, s19, 19
	s_and_b32 s39, s12, 0x380000
	s_lshl_b64 s[12:13], s[8:9], 22
	s_add_u32 s12, s16, s12
	s_addc_u32 s13, s17, s13
	s_add_u32 s12, s12, s39
	s_addc_u32 s13, s13, 0
	s_add_u32 s12, s12, s31
	s_addc_u32 s13, s13, 0
	s_add_u32 s12, s12, 0x24dff000
	s_addc_u32 s13, s13, 0
	s_mov_b64 s[56:57], 0

.LBB0_879:
	s_lshl_b64 s[54:55], s[54:55], 13
	s_add_u32 s8, s12, s54
	s_addc_u32 s12, s13, s55
	s_lshl_b32 s9, s19, s9
	s_and_b32 s9, s9, 0x700
	s_lshl_b32 s9, s9, 2
	s_add_u32 s8, s8, s9
	s_addc_u32 s9, s12, 0
	s_cmp_gt_i32 s58, s59
	s_cselect_b64 s[12:13], -1, 0
	v_cndmask_b32_e64 v8, v180, 0, s[12:13]
	s_and_b64 s[12:13], s[12:13], exec
	s_cselect_b32 s12, 0, 0x800
	v_lshlrev_b32_e32 v86, 2, v8
	v_lshl_add_u64 v[16:17], s[8:9], 0, v[86:87]
	v_mad_i64_i32 v[8:9], s[8:9], s12, v181, 0
	v_mad_i64_i32 v[10:11], s[8:9], s12, v182, 0
	v_lshl_add_u64 v[8:9], v[8:9], 2, v[16:17]
	v_lshl_add_u64 v[10:11], v[10:11], 2, v[16:17]
	global_load_dwordx4 v[24:27], v[8:9], off
	global_load_dwordx4 v[28:31], v[10:11], off
	v_mad_i64_i32 v[8:9], s[8:9], s12, v183, 0
	v_mad_i64_i32 v[10:11], s[8:9], s12, v184, 0
	v_lshl_add_u64 v[8:9], v[8:9], 2, v[16:17]
	v_lshl_add_u64 v[10:11], v[10:11], 2, v[16:17]
	global_load_dwordx4 v[32:35], v[8:9], off
	global_load_dwordx4 v[36:39], v[10:11], off
	v_mad_i64_i32 v[8:9], s[8:9], s12, v185, 0
	v_mad_i64_i32 v[10:11], s[8:9], s12, v186, 0
	v_mad_i64_i32 v[18:19], s[8:9], s12, v187, 0
	v_mad_i64_i32 v[20:21], s[8:9], s12, v188, 0
	v_lshl_add_u64 v[8:9], v[8:9], 2, v[16:17]
	v_lshl_add_u64 v[12:13], v[10:11], 2, v[16:17]
	v_lshl_add_u64 v[18:19], v[18:19], 2, v[16:17]
	v_lshl_add_u64 v[20:21], v[20:21], 2, v[16:17]
	global_load_dwordx4 v[8:11], v[8:9], off
	s_nop 0
	global_load_dwordx4 v[12:15], v[12:13], off
	s_nop 0
	global_load_dwordx4 v[16:19], v[18:19], off
	s_nop 0
	global_load_dwordx4 v[20:23], v[20:21], off
	s_cmp_gt_i32 s62, -3
	s_cselect_b32 s8, s33, 0
	s_min_i32 s8, s8, s59
	s_mul_i32 s8, s8, s3
	s_add_i32 s9, s8, s2
	s_mul_hi_i32 s8, s9, 0x2aaaaaab
	s_lshr_b32 s12, s8, 31
	s_ashr_i32 s8, s8, 7
	s_add_i32 s12, s8, s12
	s_add_i32 s8, s12, 10
	s_mulk_i32 s12, 0x300
	s_sub_i32 s19, s9, s12
	s_ashr_i32 s9, s8, 31
	s_cmpk_gt_i32 s19, 0x1ff
	s_mov_b64 s[54:55], -1
	s_cbranch_scc0 .LBB0_881
	s_lshl_b32 s12, s19, 3
	s_and_b32 s31, s12, 0x7fffffc0
	s_lshl_b32 s12, s19, 19
	s_and_b32 s33, s12, 0x380000
	s_lshl_b64 s[12:13], s[8:9], 22
	s_add_u32 s12, s16, s12
	s_addc_u32 s13, s17, s13
	s_add_u32 s12, s12, s33
	s_addc_u32 s13, s13, 0
	s_add_u32 s12, s12, s31
	s_addc_u32 s13, s13, 0
	s_add_u32 s12, s12, 0x24dff000
	s_addc_u32 s13, s13, 0
	s_mov_b64 s[54:55], 0

.LBB0_887:
	s_lshl_b64 s[12:13], s[12:13], 13
	s_add_u32 s6, s8, s12
	s_addc_u32 s8, s9, s13
	s_lshl_b32 s7, s31, s7
	s_and_b32 s7, s7, 0x700
	s_lshl_b32 s7, s7, 2
	s_add_u32 s6, s6, s7
	s_addc_u32 s7, s8, 0
	s_cmp_gt_i32 s19, s59
	s_cselect_b64 s[8:9], -1, 0
	v_cndmask_b32_e64 v40, v180, 0, s[8:9]
	s_and_b64 s[8:9], s[8:9], exec
	s_cselect_b32 s8, 0, 0x800
	v_lshlrev_b32_e32 v86, 2, v40
	v_lshl_add_u64 v[56:57], s[6:7], 0, v[86:87]
	v_mad_i64_i32 v[40:41], s[6:7], s8, v181, 0
	v_mad_i64_i32 v[42:43], s[6:7], s8, v182, 0
	v_lshl_add_u64 v[40:41], v[40:41], 2, v[56:57]
	v_lshl_add_u64 v[42:43], v[42:43], 2, v[56:57]
	global_load_dwordx4 v[48:51], v[40:41], off
	global_load_dwordx4 v[52:55], v[42:43], off
	v_mad_i64_i32 v[40:41], s[6:7], s8, v183, 0
	v_mad_i64_i32 v[42:43], s[6:7], s8, v184, 0
	v_lshl_add_u64 v[40:41], v[40:41], 2, v[56:57]
	v_lshl_add_u64 v[42:43], v[42:43], 2, v[56:57]
	global_load_dwordx4 v[64:67], v[40:41], off
	global_load_dwordx4 v[68:71], v[42:43], off
	v_mad_i64_i32 v[40:41], s[6:7], s8, v185, 0
	v_mad_i64_i32 v[42:43], s[6:7], s8, v186, 0
	v_mad_i64_i32 v[58:59], s[6:7], s8, v187, 0
	v_mad_i64_i32 v[60:61], s[6:7], s8, v188, 0
	v_lshl_add_u64 v[40:41], v[40:41], 2, v[56:57]
	v_lshl_add_u64 v[44:45], v[42:43], 2, v[56:57]
	v_lshl_add_u64 v[58:59], v[58:59], 2, v[56:57]
	v_lshl_add_u64 v[60:61], v[60:61], 2, v[56:57]
	global_load_dwordx4 v[40:43], v[40:41], off
	s_nop 0
	global_load_dwordx4 v[44:47], v[44:45], off
	s_nop 0
	global_load_dwordx4 v[56:59], v[58:59], off
	s_nop 0
	global_load_dwordx4 v[60:63], v[60:61], off
	s_cmp_gt_i32 s62, -4
	s_cselect_b32 s6, s77, 0
	s_min_i32 s6, s6, s59
	s_mul_i32 s6, s6, s3
	s_add_i32 s7, s6, s2
	s_mul_hi_i32 s6, s7, 0x2aaaaaab
	s_lshr_b32 s8, s6, 31
	s_ashr_i32 s6, s6, 7
	s_add_i32 s8, s6, s8
	s_add_i32 s6, s8, 10
	s_mulk_i32 s8, 0x300
	s_sub_i32 s19, s7, s8
	s_ashr_i32 s7, s6, 31
	s_cmpk_gt_i32 s19, 0x1ff
	s_mov_b64 s[12:13], -1
	s_cbranch_scc0 .LBB0_889
	s_lshl_b32 s8, s19, 3
	s_and_b32 s12, s8, 0x7fffffc0
	s_lshl_b32 s8, s19, 19
	s_and_b32 s13, s8, 0x380000
	s_lshl_b64 s[8:9], s[6:7], 22
	s_add_u32 s8, s16, s8
	s_addc_u32 s9, s17, s9
	s_add_u32 s8, s8, s13
	s_addc_u32 s9, s9, 0
	s_add_u32 s8, s8, s12
	s_addc_u32 s9, s9, 0
	s_add_u32 s8, s8, 0x24dff000
	s_addc_u32 s9, s9, 0
	s_mov_b64 s[12:13], 0

.LBB0_897:
	s_lshl_b64 s[8:9], s[8:9], 13
	s_add_u32 s4, s6, s8
	s_addc_u32 s6, s7, s9
	s_lshl_b32 s5, s31, s5
	s_and_b32 s5, s5, 0x700
	s_lshl_b32 s5, s5, 2
	s_add_u32 s4, s4, s5
	s_addc_u32 s5, s6, 0
	s_cmp_gt_i32 s19, s59
	s_cselect_b64 s[6:7], -1, 0
	v_cndmask_b32_e64 v8, v180, 0, s[6:7]
	s_and_b64 s[6:7], s[6:7], exec
	s_cselect_b32 s6, 0, 0x800
	v_lshlrev_b32_e32 v86, 2, v8
	v_lshl_add_u64 v[24:25], s[4:5], 0, v[86:87]
	v_mad_i64_i32 v[8:9], s[4:5], s6, v181, 0
	v_mad_i64_i32 v[10:11], s[4:5], s6, v182, 0
	v_lshl_add_u64 v[8:9], v[8:9], 2, v[24:25]
	v_lshl_add_u64 v[10:11], v[10:11], 2, v[24:25]
	global_load_dwordx4 v[20:23], v[8:9], off
	global_load_dwordx4 v[16:19], v[10:11], off
	v_mad_i64_i32 v[8:9], s[4:5], s6, v183, 0
	v_mad_i64_i32 v[10:11], s[4:5], s6, v184, 0
	v_lshl_add_u64 v[8:9], v[8:9], 2, v[24:25]
	v_lshl_add_u64 v[10:11], v[10:11], 2, v[24:25]
	global_load_dwordx4 v[36:39], v[8:9], off
	global_load_dwordx4 v[32:35], v[10:11], off
	v_mad_i64_i32 v[8:9], s[4:5], s6, v185, 0
	v_mad_i64_i32 v[10:11], s[4:5], s6, v186, 0
	v_mad_i64_i32 v[26:27], s[4:5], s6, v187, 0
	v_mad_i64_i32 v[28:29], s[4:5], s6, v188, 0
	v_lshl_add_u64 v[8:9], v[8:9], 2, v[24:25]
	v_lshl_add_u64 v[10:11], v[10:11], 2, v[24:25]
	v_lshl_add_u64 v[26:27], v[26:27], 2, v[24:25]
	v_lshl_add_u64 v[24:25], v[28:29], 2, v[24:25]
	global_load_dwordx4 v[12:15], v[8:9], off
	s_nop 0
	global_load_dwordx4 v[8:11], v[10:11], off
	s_nop 0
	global_load_dwordx4 v[28:31], v[26:27], off
	s_nop 0
	global_load_dwordx4 v[24:27], v[24:25], off
	s_cmp_gt_i32 s62, -5
	s_cselect_b32 s4, s78, 0
	s_min_i32 s4, s4, s59
	s_mul_i32 s4, s4, s3
	s_add_i32 s5, s4, s2
	s_mul_hi_i32 s4, s5, 0x2aaaaaab
	s_lshr_b32 s6, s4, 31
	s_ashr_i32 s4, s4, 7
	s_add_i32 s6, s4, s6
	s_add_i32 s4, s6, 10
	s_mulk_i32 s6, 0x300
	s_sub_i32 s12, s5, s6
	s_ashr_i32 s5, s4, 31
	s_cmpk_gt_i32 s12, 0x1ff
	s_mov_b64 s[8:9], -1
	s_cbranch_scc0 .LBB0_899
	s_lshl_b32 s6, s12, 3
	s_and_b32 s8, s6, 0x7fffffc0
	s_lshl_b32 s6, s12, 19
	s_and_b32 s9, s6, 0x380000
	s_lshl_b64 s[6:7], s[4:5], 22
	s_add_u32 s6, s16, s6
	s_addc_u32 s7, s17, s7
	s_add_u32 s6, s6, s9
	s_addc_u32 s7, s7, 0
	s_add_u32 s6, s6, s8
	s_addc_u32 s7, s7, 0
	s_add_u32 s6, s6, 0x24dff000
	s_addc_u32 s7, s7, 0
	s_mov_b64 s[8:9], 0

.LBB0_943:
	s_lshl_b64 s[4:5], s[8:9], 13
	s_add_u32 s4, s6, s4
	s_addc_u32 s5, s7, s5
	s_lshl_b32 s0, s22, s0
	s_and_b32 s0, s0, 0x700
	s_lshl_b32 s0, s0, 2
	s_add_u32 s4, s4, s0
	s_addc_u32 s5, s5, 0
	s_cmp_gt_i32 s62, s59
	s_cselect_b64 s[6:7], -1, 0
	v_cndmask_b32_e64 v0, v180, 0, s[6:7]
	s_and_b64 s[6:7], s[6:7], exec
	s_cselect_b32 s0, 0, 0x800
	v_lshlrev_b32_e32 v102, 2, v0
	v_lshl_add_u64 v[88:89], s[4:5], 0, v[102:103]
	v_mad_i64_i32 v[0:1], s[4:5], s0, v181, 0
	v_lshl_add_u64 v[72:73], v[0:1], 2, v[88:89]
	v_mad_i64_i32 v[0:1], s[4:5], s0, v182, 0
	v_lshl_add_u64 v[74:75], v[0:1], 2, v[88:89]
	global_load_dwordx4 v[0:3], v[72:73], off
	global_load_dwordx4 v[4:7], v[74:75], off
	v_mad_i64_i32 v[72:73], s[4:5], s0, v183, 0
	v_lshl_add_u64 v[80:81], v[72:73], 2, v[88:89]
	v_mad_i64_i32 v[72:73], s[4:5], s0, v184, 0
	v_lshl_add_u64 v[82:83], v[72:73], 2, v[88:89]
	global_load_dwordx4 v[72:75], v[80:81], off
	global_load_dwordx4 v[76:79], v[82:83], off
	v_mad_i64_i32 v[80:81], s[4:5], s0, v185, 0
	v_lshl_add_u64 v[90:91], v[80:81], 2, v[88:89]
	v_mad_i64_i32 v[80:81], s[4:5], s0, v186, 0
	v_lshl_add_u64 v[92:93], v[80:81], 2, v[88:89]
	global_load_dwordx4 v[80:83], v[90:91], off
	global_load_dwordx4 v[84:87], v[92:93], off
	v_mad_i64_i32 v[90:91], s[4:5], s0, v187, 0
	v_lshl_add_u64 v[96:97], v[90:91], 2, v[88:89]
	v_mad_i64_i32 v[90:91], s[4:5], s0, v188, 0
	v_lshl_add_u64 v[98:99], v[90:91], 2, v[88:89]
	global_load_dwordx4 v[88:91], v[96:97], off
	global_load_dwordx4 v[92:95], v[98:99], off
	s_max_i32 s0, s62, 3
	s_add_i32 s0, s0, -3
	s_min_i32 s0, s0, s59
	s_mul_i32 s0, s0, s3
	s_add_i32 s0, s0, s2
	s_mul_hi_i32 s4, s0, 0x2aaaaaab
	s_lshr_b32 s5, s4, 31
	s_ashr_i32 s4, s4, 7
	s_add_i32 s5, s4, s5
	s_add_i32 s4, s5, 10
	s_mulk_i32 s5, 0x300
	s_sub_i32 s0, s0, s5
	s_ashr_i32 s5, s4, 31
	s_cmpk_gt_i32 s0, 0x1ff
	s_mov_b64 s[8:9], -1
	s_cbranch_scc0 .LBB0_945
	s_lshl_b32 s6, s0, 3
	s_and_b32 s8, s6, 0x7fffffc0
	s_lshl_b32 s6, s0, 19
	s_and_b32 s9, s6, 0x380000
	s_lshl_b64 s[6:7], s[4:5], 22
	s_add_u32 s6, s16, s6
	s_addc_u32 s7, s17, s7
	s_add_u32 s6, s6, s9
	s_addc_u32 s7, s7, 0
	s_add_u32 s6, s6, s8
	s_addc_u32 s7, s7, 0
	s_add_u32 s6, s6, 0x24dff000
	s_addc_u32 s7, s7, 0
	s_mov_b64 s[8:9], 0

.LBB0_953:
	s_lshl_b64 s[4:5], s[8:9], 13
	s_add_u32 s4, s6, s4
	s_addc_u32 s5, s7, s5
	s_lshl_b32 s0, s22, s0
	s_and_b32 s0, s0, 0x700
	s_lshl_b32 s0, s0, 2
	s_add_u32 s4, s4, s0
	s_addc_u32 s5, s5, 0
	s_cmp_gt_i32 s62, s59
	s_cselect_b64 s[6:7], -1, 0
	v_cndmask_b32_e64 v0, v180, 0, s[6:7]
	s_and_b64 s[6:7], s[6:7], exec
	s_cselect_b32 s0, 0, 0x800
	v_lshlrev_b32_e32 v102, 2, v0
	v_lshl_add_u64 v[0:1], s[4:5], 0, v[102:103]
	v_mad_i64_i32 v[2:3], s[4:5], s0, v181, 0
	v_lshl_add_u64 v[2:3], v[2:3], 2, v[0:1]
	v_mad_i64_i32 v[4:5], s[4:5], s0, v182, 0
	v_lshl_add_u64 v[4:5], v[4:5], 2, v[0:1]
	global_load_dwordx4 v[48:51], v[2:3], off
	global_load_dwordx4 v[52:55], v[4:5], off
	v_mad_i64_i32 v[2:3], s[4:5], s0, v183, 0
	v_lshl_add_u64 v[2:3], v[2:3], 2, v[0:1]
	v_mad_i64_i32 v[4:5], s[4:5], s0, v184, 0
	v_lshl_add_u64 v[4:5], v[4:5], 2, v[0:1]
	global_load_dwordx4 v[64:67], v[2:3], off
	global_load_dwordx4 v[68:71], v[4:5], off
	v_mad_i64_i32 v[2:3], s[4:5], s0, v185, 0
	v_lshl_add_u64 v[2:3], v[2:3], 2, v[0:1]
	v_mad_i64_i32 v[4:5], s[4:5], s0, v186, 0
	v_lshl_add_u64 v[4:5], v[4:5], 2, v[0:1]
	global_load_dwordx4 v[40:43], v[2:3], off
	global_load_dwordx4 v[44:47], v[4:5], off
	v_mad_i64_i32 v[2:3], s[4:5], s0, v187, 0
	v_lshl_add_u64 v[2:3], v[2:3], 2, v[0:1]
	v_mad_i64_i32 v[4:5], s[4:5], s0, v188, 0
	v_lshl_add_u64 v[0:1], v[4:5], 2, v[0:1]
	global_load_dwordx4 v[56:59], v[2:3], off
	global_load_dwordx4 v[60:63], v[0:1], off
	s_max_i32 s0, s62, 3
	s_add_i32 s0, s0, -3
	s_min_i32 s0, s0, s59
	s_mul_i32 s0, s0, s3
	s_add_i32 s0, s0, s2
	s_mul_hi_i32 s4, s0, 0x2aaaaaab
	s_lshr_b32 s5, s4, 31
	s_ashr_i32 s4, s4, 7
	s_add_i32 s5, s4, s5
	s_add_i32 s4, s5, 10
	s_mulk_i32 s5, 0x300
	s_sub_i32 s0, s0, s5
	s_ashr_i32 s5, s4, 31
	s_cmpk_gt_i32 s0, 0x1ff
	s_mov_b64 s[8:9], -1
	s_cbranch_scc0 .LBB0_955
	s_lshl_b32 s6, s0, 3
	s_and_b32 s8, s6, 0x7fffffc0
	s_lshl_b32 s6, s0, 19
	s_and_b32 s9, s6, 0x380000
	s_lshl_b64 s[6:7], s[4:5], 22
	s_add_u32 s6, s16, s6
	s_addc_u32 s7, s17, s7
	s_add_u32 s6, s6, s9
	s_addc_u32 s7, s7, 0
	s_add_u32 s6, s6, s8
	s_addc_u32 s7, s7, 0
	s_add_u32 s6, s6, 0x24dff000
	s_addc_u32 s7, s7, 0
	s_mov_b64 s[8:9], 0
